# v55 + the second of the two back-to-back barriers at each P2a step-loop exit removed (A stages are per-wave private; nothing reads LDS before the next prologue barrier)
# speedup vs baseline: 1.0090x; 1.0090x over previous
.Lmy_tl_267_3:
	v_mfma_f32_16x16x32_bf16 v[2:5], v[182:185], v[152:155], v[2:5]
	v_mfma_f32_16x16x32_bf16 v[26:29], v[182:185], v[156:159], v[26:29]
	s_waitcnt lgkmcnt(0)
	s_barrier
	s_mov_b32 s50, s77
	s_cbranch_vccnz .LBB0_267
	s_waitcnt vmcnt(0)
	s_waitcnt lgkmcnt(0)
	s_mov_b64 s[10:11], 0
	s_branch .LBB0_274

.Lmy_tl_272_3:
	v_mfma_f32_16x16x32_bf16 v[2:5], v[116:119], v[136:139], v[2:5]
	s_waitcnt lgkmcnt(0)
	s_barrier
	s_mov_b32 s52, s75
	s_cbranch_vccnz .LBB0_272
	s_waitcnt vmcnt(0)
	s_waitcnt lgkmcnt(0)
	v_mov_b32_e32 v81, 0
	v_mov_b32_e32 v80, v81
	v_mov_b32_e32 v79, v81
	v_mov_b32_e32 v78, v81
	v_mov_b32_e32 v61, v81
	v_mov_b32_e32 v60, v81
	v_mov_b32_e32 v59, v81
	v_mov_b32_e32 v58, v81
	v_mov_b32_e32 v41, v81
	v_mov_b32_e32 v40, v81
	v_mov_b32_e32 v39, v81
	v_mov_b32_e32 v38, v81
	v_mov_b32_e32 v25, v81
	v_mov_b32_e32 v24, v81
	v_mov_b32_e32 v23, v81
	v_mov_b32_e32 v22, v81
	v_mov_b32_e32 v85, v81
	v_mov_b32_e32 v84, v81
	v_mov_b32_e32 v83, v81
	v_mov_b32_e32 v82, v81
	v_mov_b32_e32 v69, v81
	v_mov_b32_e32 v68, v81
	v_mov_b32_e32 v67, v81
	v_mov_b32_e32 v66, v81
	v_mov_b32_e32 v53, v81
	v_mov_b32_e32 v52, v81
	v_mov_b32_e32 v51, v81
	v_mov_b32_e32 v50, v81
	v_mov_b32_e32 v29, v81
	v_mov_b32_e32 v28, v81
	v_mov_b32_e32 v27, v81
	v_mov_b32_e32 v26, v81

.Lmy_tl_279_3:
	v_mfma_f32_16x16x32_bf16 v[2:5], v[224:227], v[200:203], v[2:5]
	v_mfma_f32_16x16x32_bf16 v[26:29], v[224:227], v[204:207], v[26:29]
	v_mfma_f32_16x16x32_bf16 v[98:101], v[224:227], v[208:211], v[98:101]
	s_waitcnt lgkmcnt(0)
	s_barrier
	s_mov_b32 s48, s79
	s_cbranch_vccnz .LBB0_279
	s_waitcnt vmcnt(0)
	s_waitcnt lgkmcnt(0)
	s_mov_b64 s[8:9], 0

.Lmy_tl_283_3:
	s_waitcnt lgkmcnt(0)
	s_barrier
	s_mov_b32 s50, s51
	s_cbranch_vccnz .LBB0_283
	s_waitcnt vmcnt(0)
	s_waitcnt lgkmcnt(0)
	v_mov_b32_e32 v77, 0
	v_mov_b32_e32 v76, v77
	v_mov_b32_e32 v75, v77
	v_mov_b32_e32 v74, v77
	v_mov_b32_e32 v81, v77
	v_mov_b32_e32 v80, v77
	v_mov_b32_e32 v79, v77
	v_mov_b32_e32 v78, v77
	v_mov_b32_e32 v125, v77
	v_mov_b32_e32 v124, v77
	v_mov_b32_e32 v123, v77
	v_mov_b32_e32 v122, v77
	v_mov_b32_e32 v49, v77
	v_mov_b32_e32 v48, v77
	v_mov_b32_e32 v47, v77
	v_mov_b32_e32 v46, v77
	v_mov_b32_e32 v61, v77
	v_mov_b32_e32 v60, v77
	v_mov_b32_e32 v59, v77
	v_mov_b32_e32 v58, v77
	v_mov_b32_e32 v117, v77
	v_mov_b32_e32 v116, v77
	v_mov_b32_e32 v115, v77
	v_mov_b32_e32 v114, v77
	v_mov_b32_e32 v21, v77
	v_mov_b32_e32 v20, v77
	v_mov_b32_e32 v19, v77
	v_mov_b32_e32 v18, v77
	v_mov_b32_e32 v41, v77
	v_mov_b32_e32 v40, v77
	v_mov_b32_e32 v39, v77
	v_mov_b32_e32 v38, v77
	v_mov_b32_e32 v109, v77
	v_mov_b32_e32 v108, v77
	v_mov_b32_e32 v107, v77
	v_mov_b32_e32 v106, v77
	v_mov_b32_e32 v9, v77
	v_mov_b32_e32 v8, v77
	v_mov_b32_e32 v7, v77
	v_mov_b32_e32 v6, v77
	v_mov_b32_e32 v25, v77
	v_mov_b32_e32 v24, v77
	v_mov_b32_e32 v23, v77
	v_mov_b32_e32 v22, v77
	v_mov_b32_e32 v105, v77
	v_mov_b32_e32 v104, v77
	v_mov_b32_e32 v103, v77
	v_mov_b32_e32 v102, v77
	v_mov_b32_e32 v57, v77
	v_mov_b32_e32 v56, v77
	v_mov_b32_e32 v55, v77
	v_mov_b32_e32 v54, v77
	v_mov_b32_e32 v85, v77
	v_mov_b32_e32 v84, v77
	v_mov_b32_e32 v83, v77
	v_mov_b32_e32 v82, v77
	v_mov_b32_e32 v129, v77
	v_mov_b32_e32 v128, v77
	v_mov_b32_e32 v127, v77
	v_mov_b32_e32 v126, v77
	v_mov_b32_e32 v37, v77
	v_mov_b32_e32 v36, v77
	v_mov_b32_e32 v35, v77
	v_mov_b32_e32 v34, v77
	v_mov_b32_e32 v69, v77
	v_mov_b32_e32 v68, v77
	v_mov_b32_e32 v67, v77
	v_mov_b32_e32 v66, v77
	v_mov_b32_e32 v121, v77
	v_mov_b32_e32 v120, v77
	v_mov_b32_e32 v119, v77
	v_mov_b32_e32 v118, v77
	v_mov_b32_e32 v17, v77
	v_mov_b32_e32 v16, v77
	v_mov_b32_e32 v15, v77
	v_mov_b32_e32 v14, v77
	v_mov_b32_e32 v53, v77
	v_mov_b32_e32 v52, v77
	v_mov_b32_e32 v51, v77
	v_mov_b32_e32 v50, v77
	v_mov_b32_e32 v113, v77
	v_mov_b32_e32 v112, v77
	v_mov_b32_e32 v111, v77
	v_mov_b32_e32 v110, v77
	v_mov_b32_e32 v5, v77
	v_mov_b32_e32 v4, v77
	v_mov_b32_e32 v3, v77
	v_mov_b32_e32 v2, v77
	v_mov_b32_e32 v29, v77
	v_mov_b32_e32 v28, v77
	v_mov_b32_e32 v27, v77
	v_mov_b32_e32 v26, v77
	v_mov_b32_e32 v101, v77
	v_mov_b32_e32 v100, v77
	v_mov_b32_e32 v99, v77
	v_mov_b32_e32 v98, v77

.Lmy_tl_873_3:
	v_mfma_f32_16x16x32_bf16 v[2:5], v[182:185], v[152:155], v[2:5]
	v_mfma_f32_16x16x32_bf16 v[26:29], v[182:185], v[156:159], v[26:29]
	s_waitcnt lgkmcnt(0)
	s_barrier
	s_mov_b32 s48, s77
	s_cbranch_vccnz .LBB0_873
	s_waitcnt vmcnt(0)
	s_waitcnt lgkmcnt(0)
	s_mov_b64 s[14:15], 0
	s_branch .LBB0_880

.Lmy_tl_878_3:
	v_mfma_f32_16x16x32_bf16 v[2:5], v[116:119], v[136:139], v[2:5]
	s_waitcnt lgkmcnt(0)
	s_barrier
	s_mov_b32 s50, s75
	s_cbranch_vccnz .LBB0_878
	s_waitcnt vmcnt(0)
	s_waitcnt lgkmcnt(0)
	v_mov_b32_e32 v81, 0
	v_mov_b32_e32 v80, v81
	v_mov_b32_e32 v79, v81
	v_mov_b32_e32 v78, v81
	v_mov_b32_e32 v61, v81
	v_mov_b32_e32 v60, v81
	v_mov_b32_e32 v59, v81
	v_mov_b32_e32 v58, v81
	v_mov_b32_e32 v41, v81
	v_mov_b32_e32 v40, v81
	v_mov_b32_e32 v39, v81
	v_mov_b32_e32 v38, v81
	v_mov_b32_e32 v25, v81
	v_mov_b32_e32 v24, v81
	v_mov_b32_e32 v23, v81
	v_mov_b32_e32 v22, v81
	v_mov_b32_e32 v85, v81
	v_mov_b32_e32 v84, v81
	v_mov_b32_e32 v83, v81
	v_mov_b32_e32 v82, v81
	v_mov_b32_e32 v69, v81
	v_mov_b32_e32 v68, v81
	v_mov_b32_e32 v67, v81
	v_mov_b32_e32 v66, v81
	v_mov_b32_e32 v53, v81
	v_mov_b32_e32 v52, v81
	v_mov_b32_e32 v51, v81
	v_mov_b32_e32 v50, v81
	v_mov_b32_e32 v29, v81
	v_mov_b32_e32 v28, v81
	v_mov_b32_e32 v27, v81
	v_mov_b32_e32 v26, v81

.Lmy_tl_885_3:
	v_mfma_f32_16x16x32_bf16 v[2:5], v[216:219], v[200:203], v[2:5]
	v_mfma_f32_16x16x32_bf16 v[26:29], v[216:219], v[204:207], v[26:29]
	v_mfma_f32_16x16x32_bf16 v[98:101], v[216:219], v[208:211], v[98:101]
	s_waitcnt lgkmcnt(0)
	s_barrier
	s_mov_b32 s46, s80
	s_cbranch_vccnz .LBB0_885
	s_waitcnt vmcnt(0)
	s_waitcnt lgkmcnt(0)
	s_mov_b64 s[12:13], 0

.Lmy_tl_889_3:
	s_waitcnt lgkmcnt(0)
	s_barrier
	s_mov_b32 s48, s49
	s_cbranch_vccnz .LBB0_889
	s_waitcnt vmcnt(0)
	s_waitcnt lgkmcnt(0)
	v_mov_b32_e32 v77, 0
	v_mov_b32_e32 v76, v77
	v_mov_b32_e32 v75, v77
	v_mov_b32_e32 v74, v77
	v_mov_b32_e32 v81, v77
	v_mov_b32_e32 v80, v77
	v_mov_b32_e32 v79, v77
	v_mov_b32_e32 v78, v77
	v_mov_b32_e32 v125, v77
	v_mov_b32_e32 v124, v77
	v_mov_b32_e32 v123, v77
	v_mov_b32_e32 v122, v77
	v_mov_b32_e32 v49, v77
	v_mov_b32_e32 v48, v77
	v_mov_b32_e32 v47, v77
	v_mov_b32_e32 v46, v77
	v_mov_b32_e32 v61, v77
	v_mov_b32_e32 v60, v77
	v_mov_b32_e32 v59, v77
	v_mov_b32_e32 v58, v77
	v_mov_b32_e32 v117, v77
	v_mov_b32_e32 v116, v77
	v_mov_b32_e32 v115, v77
	v_mov_b32_e32 v114, v77
	v_mov_b32_e32 v21, v77
	v_mov_b32_e32 v20, v77
	v_mov_b32_e32 v19, v77
	v_mov_b32_e32 v18, v77
	v_mov_b32_e32 v41, v77
	v_mov_b32_e32 v40, v77
	v_mov_b32_e32 v39, v77
	v_mov_b32_e32 v38, v77
	v_mov_b32_e32 v109, v77
	v_mov_b32_e32 v108, v77
	v_mov_b32_e32 v107, v77
	v_mov_b32_e32 v106, v77
	v_mov_b32_e32 v9, v77
	v_mov_b32_e32 v8, v77
	v_mov_b32_e32 v7, v77
	v_mov_b32_e32 v6, v77
	v_mov_b32_e32 v25, v77
	v_mov_b32_e32 v24, v77
	v_mov_b32_e32 v23, v77
	v_mov_b32_e32 v22, v77
	v_mov_b32_e32 v105, v77
	v_mov_b32_e32 v104, v77
	v_mov_b32_e32 v103, v77
	v_mov_b32_e32 v102, v77
	v_mov_b32_e32 v57, v77
	v_mov_b32_e32 v56, v77
	v_mov_b32_e32 v55, v77
	v_mov_b32_e32 v54, v77
	v_mov_b32_e32 v85, v77
	v_mov_b32_e32 v84, v77
	v_mov_b32_e32 v83, v77
	v_mov_b32_e32 v82, v77
	v_mov_b32_e32 v129, v77
	v_mov_b32_e32 v128, v77
	v_mov_b32_e32 v127, v77
	v_mov_b32_e32 v126, v77
	v_mov_b32_e32 v37, v77
	v_mov_b32_e32 v36, v77
	v_mov_b32_e32 v35, v77
	v_mov_b32_e32 v34, v77
	v_mov_b32_e32 v69, v77
	v_mov_b32_e32 v68, v77
	v_mov_b32_e32 v67, v77
	v_mov_b32_e32 v66, v77
	v_mov_b32_e32 v121, v77
	v_mov_b32_e32 v120, v77
	v_mov_b32_e32 v119, v77
	v_mov_b32_e32 v118, v77
	v_mov_b32_e32 v17, v77
	v_mov_b32_e32 v16, v77
	v_mov_b32_e32 v15, v77
	v_mov_b32_e32 v14, v77
	v_mov_b32_e32 v53, v77
	v_mov_b32_e32 v52, v77
	v_mov_b32_e32 v51, v77
	v_mov_b32_e32 v50, v77
	v_mov_b32_e32 v113, v77
	v_mov_b32_e32 v112, v77
	v_mov_b32_e32 v111, v77
	v_mov_b32_e32 v110, v77
	v_mov_b32_e32 v5, v77
	v_mov_b32_e32 v4, v77
	v_mov_b32_e32 v3, v77
	v_mov_b32_e32 v2, v77
	v_mov_b32_e32 v29, v77
	v_mov_b32_e32 v28, v77
	v_mov_b32_e32 v27, v77
	v_mov_b32_e32 v26, v77
	v_mov_b32_e32 v101, v77
	v_mov_b32_e32 v100, v77
	v_mov_b32_e32 v99, v77
	v_mov_b32_e32 v98, v77
